# scores softmax epilogue: rolling prefetch (3 deep, counted lgkmcnt) of the per-row statistics reads in its three passes instead of a serial LDS round trip per row block
# baseline (speedup 1.0000x reference)
; #define PG8_LAS __attribute__((address_space(3)))
;     __device__ __forceinline__ void operator()(f32x4 (&acc)[2][2][4][2], const Unit& u, int wr, int wc, int fr, int fq) const {
;     ...
;             for (int m = 0; m < 4; ++m) { float t = -3.0e38f;
;                 const f32x4 s4 = *(PG8_LAS const f32x4*)(ss + (ai * HALF + wr * 64 + m * 16 + fr) * 4);
;                 const float rs = rsqrtf(((s4[0] + s4[1]) + (s4[2] + s4[3])) * (1.f / D) + 1e-6f);
; #pragma unroll
;                 for (int bj = 0; bj < 2; ++bj)
; #pragma unroll
;                     for (int n = 0; n < 2; ++n) { acc[ai][bj][m][n] = acc[ai][bj][m][n] * rs; const f32x4 v = acc[ai][bj][m][n]; t = fmaxf(t, fmaxf(fmaxf(v[0], v[1]), fmaxf(v[2], v[3]))); }
;                 t = rows_max4(t);
;                 if (fq == 0) smax[(ai * HALF + wr * 64 + m * 16 + fr) * 4 + wc] = t; }
.LBB0_2073:
	ds_read_b128 v[222:225], v201
	ds_read_b128 v[226:229], v203
	ds_read_b128 v[230:233], v204
	s_waitcnt lgkmcnt(2)
	v_mov_b32_e32 v140, v222
	v_mov_b32_e32 v141, v223
	v_mov_b32_e32 v142, v224
	v_mov_b32_e32 v143, v225
	ds_read_b128 v[222:225], v205
	v_mov_b32_e32 v144, v141
	v_mov_b32_e32 v145, v142
	v_mov_b32_e32 v141, v143
	v_pk_add_f32 v[140:141], v[144:145], v[140:141]
	s_nop 0
	v_add_f32_e32 v140, v140, v141
	v_fmamk_f32 v140, v140, 0x3a800000, v194
	v_mul_f32_e32 v141, 0x4b800000, v140
	v_cmp_gt_f32_e32 vcc, s64, v140
	s_nop 1
	v_cndmask_b32_e32 v140, v140, v141, vcc
	v_rsq_f32_e32 v140, v140
	s_nop 0
	v_mul_f32_e32 v141, 0x45800000, v140
	v_cndmask_b32_e32 v142, v140, v141, vcc
	v_pk_mul_f32 v[190:191], v[126:127], v[142:143] op_sel_hi:[1,0]
	v_pk_mul_f32 v[192:193], v[124:125], v[142:143] op_sel_hi:[1,0]
	v_pk_mul_f32 v[124:125], v[122:123], v[142:143] op_sel_hi:[1,0]
	v_pk_mul_f32 v[122:123], v[120:121], v[142:143] op_sel_hi:[1,0]
	v_max_f32_e32 v120, v190, v191
	v_max_f32_e32 v121, v124, v125
	v_pk_mul_f32 v[140:141], v[118:119], v[142:143] op_sel_hi:[1,0]
	v_pk_mul_f32 v[144:145], v[114:115], v[142:143] op_sel_hi:[1,0]
	v_max3_f32 v120, v192, v193, v120
	v_max3_f32 v121, v122, v123, v121
	v_pk_mul_f32 v[126:127], v[116:117], v[142:143] op_sel_hi:[1,0]
	v_max_f32_e32 v116, v140, v141
	v_pk_mul_f32 v[142:143], v[112:113], v[142:143] op_sel_hi:[1,0]
	v_max_f32_e32 v112, v144, v145
	v_max3_f32 v120, v120, s34, v121
	v_max3_f32 v116, v126, v127, v116
	v_max3_f32 v112, v142, v143, v112
	v_max3_f32 v112, v120, v116, v112
	v_mov_b32_e32 v113, v112
	s_nop 1
	v_permlane16_swap_b32_e32 v112, v113
	v_max_f32_e32 v113, v113, v113
	v_max_f32_e32 v112, v112, v112
	v_max_f32_e32 v112, v112, v113
	v_mov_b32_e32 v113, v112
	s_nop 1
	v_permlane32_swap_b32_e32 v112, v113
	s_and_saveexec_b64 s[22:23], s[4:5]
	v_max_f32_e32 v112, v112, v112
	v_max_f32_e32 v113, v113, v113
	v_max_f32_e32 v112, v112, v113
	ds_write_b32 v202, v112
	s_or_b64 exec, exec, s[22:23]
	s_waitcnt lgkmcnt(3)
	v_mov_b32_e32 v112, v226
	v_mov_b32_e32 v113, v227
	v_mov_b32_e32 v114, v228
	v_mov_b32_e32 v115, v229
	ds_read_b128 v[226:229], v206
	v_mov_b32_e32 v116, v113
	v_mov_b32_e32 v117, v114
	v_mov_b32_e32 v113, v115
	v_pk_add_f32 v[112:113], v[116:117], v[112:113]
	s_nop 0
	v_add_f32_e32 v112, v112, v113
	v_fmamk_f32 v112, v112, 0x3a800000, v194
	v_mul_f32_e32 v113, 0x4b800000, v112
	v_cmp_gt_f32_e32 vcc, s64, v112
	s_nop 1
	v_cndmask_b32_e32 v112, v112, v113, vcc
	v_rsq_f32_e32 v112, v112
	s_nop 0
	v_mul_f32_e32 v113, 0x45800000, v112
	v_cndmask_b32_e32 v112, v112, v113, vcc
	v_pk_mul_f32 v[186:187], v[110:111], v[112:113] op_sel_hi:[1,0]
	v_pk_mul_f32 v[180:181], v[106:107], v[112:113] op_sel_hi:[1,0]
	v_pk_mul_f32 v[178:179], v[102:103], v[112:113] op_sel_hi:[1,0]
	v_pk_mul_f32 v[188:189], v[108:109], v[112:113] op_sel_hi:[1,0]
	v_pk_mul_f32 v[184:185], v[104:105], v[112:113] op_sel_hi:[1,0]
	v_max_f32_e32 v104, v186, v187
	v_max_f32_e32 v105, v180, v181
	v_pk_mul_f32 v[182:183], v[100:101], v[112:113] op_sel_hi:[1,0]
	v_max_f32_e32 v100, v178, v179
	v_pk_mul_f32 v[106:107], v[98:99], v[112:113] op_sel_hi:[1,0]
	v_max3_f32 v104, v188, v189, v104
	v_max3_f32 v105, v184, v185, v105
	v_max3_f32 v102, v182, v183, v100
	v_pk_mul_f32 v[100:101], v[96:97], v[112:113] op_sel_hi:[1,0]
	v_max_f32_e32 v96, v106, v107
	v_max3_f32 v104, v104, s34, v105
	v_max3_f32 v96, v100, v101, v96
	v_max3_f32 v96, v104, v102, v96
	v_mov_b32_e32 v97, v96
	s_nop 1
	v_permlane16_swap_b32_e32 v96, v97
	v_max_f32_e32 v97, v97, v97
	v_max_f32_e32 v96, v96, v96
	v_max_f32_e32 v96, v96, v97
	v_mov_b32_e32 v97, v96
	s_nop 1
	v_permlane32_swap_b32_e32 v96, v97
	s_and_saveexec_b64 s[22:23], s[4:5]
	v_max_f32_e32 v96, v96, v96
	v_max_f32_e32 v97, v97, v97
	v_max_f32_e32 v96, v96, v97
	ds_write_b32 v202, v96 offset:256
	s_or_b64 exec, exec, s[22:23]
	s_waitcnt lgkmcnt(4)
	v_mov_b32_e32 v96, v230
	v_mov_b32_e32 v97, v231
	v_mov_b32_e32 v98, v232
	v_mov_b32_e32 v99, v233
	ds_read_b128 v[230:233], v207
	v_mov_b32_e32 v102, v97
	v_mov_b32_e32 v103, v98
	v_mov_b32_e32 v97, v99
	v_pk_add_f32 v[96:97], v[102:103], v[96:97]
	s_nop 0
	v_add_f32_e32 v96, v96, v97
	v_fmamk_f32 v96, v96, 0x3a800000, v194
	v_mul_f32_e32 v97, 0x4b800000, v96
	v_cmp_gt_f32_e32 vcc, s64, v96
	s_nop 1
	v_cndmask_b32_e32 v96, v96, v97, vcc
	v_rsq_f32_e32 v96, v96
	s_nop 0
	v_mul_f32_e32 v97, 0x45800000, v96
	v_cndmask_b32_e32 v96, v96, v97, vcc
	v_pk_mul_f32 v[176:177], v[94:95], v[96:97] op_sel_hi:[1,0]
	v_pk_mul_f32 v[102:103], v[90:91], v[96:97] op_sel_hi:[1,0]
	v_pk_mul_f32 v[92:93], v[92:93], v[96:97] op_sel_hi:[1,0]
	v_pk_mul_f32 v[94:95], v[88:89], v[96:97] op_sel_hi:[1,0]
	v_max_f32_e32 v88, v176, v177
	v_max_f32_e32 v89, v102, v103
	v_pk_mul_f32 v[108:109], v[86:87], v[96:97] op_sel_hi:[1,0]
	v_pk_mul_f32 v[112:113], v[82:83], v[96:97] op_sel_hi:[1,0]
	v_max3_f32 v88, v92, v93, v88
	v_max3_f32 v89, v94, v95, v89
	v_pk_mul_f32 v[104:105], v[84:85], v[96:97] op_sel_hi:[1,0]
	v_max_f32_e32 v84, v108, v109
	v_pk_mul_f32 v[110:111], v[80:81], v[96:97] op_sel_hi:[1,0]
	v_max_f32_e32 v80, v112, v113
	v_max3_f32 v88, v88, s34, v89
	v_max3_f32 v84, v104, v105, v84
	v_max3_f32 v80, v110, v111, v80
	v_max3_f32 v80, v88, v84, v80
	v_mov_b32_e32 v81, v80
	s_nop 1
	v_permlane16_swap_b32_e32 v80, v81
	v_max_f32_e32 v81, v81, v81
	v_max_f32_e32 v80, v80, v80
	v_max_f32_e32 v80, v80, v81
	v_mov_b32_e32 v81, v80
	s_nop 1
	v_permlane32_swap_b32_e32 v80, v81
	s_and_saveexec_b64 s[22:23], s[4:5]
	v_max_f32_e32 v80, v80, v80
	v_max_f32_e32 v81, v81, v81
	v_max_f32_e32 v80, v80, v81
	ds_write_b32 v202, v80 offset:512
	s_or_b64 exec, exec, s[22:23]
	s_waitcnt lgkmcnt(5)
; #define PG8_LAS __attribute__((address_space(3)))
;     __device__ __forceinline__ void operator()(f32x4 (&acc)[2][2][4][2], const Unit& u, int wr, int wc, int fr, int fq) const {
;     ...
;             for (int m = 0; m < 4; ++m) { float t = -3.0e38f;
;                 const f32x4 s4 = *(PG8_LAS const f32x4*)(ss + (ai * HALF + wr * 64 + m * 16 + fr) * 4);
;                 const float rs = rsqrtf(((s4[0] + s4[1]) + (s4[2] + s4[3])) * (1.f / D) + 1e-6f);
; #pragma unroll
;                 for (int bj = 0; bj < 2; ++bj)
; #pragma unroll
;                     for (int n = 0; n < 2; ++n) { acc[ai][bj][m][n] = acc[ai][bj][m][n] * rs; const f32x4 v = acc[ai][bj][m][n]; t = fmaxf(t, fmaxf(fmaxf(v[0], v[1]), fmaxf(v[2], v[3]))); }
;                 t = rows_max4(t);
;                 if (fq == 0) smax[(ai * HALF + wr * 64 + m * 16 + fr) * 4 + wc] = t; }
	v_mov_b32_e32 v80, v222
	v_mov_b32_e32 v81, v223
	v_mov_b32_e32 v82, v224
	v_mov_b32_e32 v83, v225
	ds_read_b128 v[222:225], v208
	v_mov_b32_e32 v84, v81
	v_mov_b32_e32 v85, v82
	v_mov_b32_e32 v81, v83
	v_pk_add_f32 v[80:81], v[84:85], v[80:81]
	s_nop 0
	v_add_f32_e32 v80, v80, v81
	v_fmamk_f32 v80, v80, 0x3a800000, v194
	v_mul_f32_e32 v81, 0x4b800000, v80
	v_cmp_gt_f32_e32 vcc, s64, v80
	s_nop 1
	v_cndmask_b32_e32 v80, v80, v81, vcc
	v_rsq_f32_e32 v80, v80
	s_nop 0
	v_mul_f32_e32 v81, 0x45800000, v80
	v_cndmask_b32_e32 v80, v80, v81, vcc
	v_pk_mul_f32 v[172:173], v[78:79], v[80:81] op_sel_hi:[1,0]
	v_pk_mul_f32 v[166:167], v[74:75], v[80:81] op_sel_hi:[1,0]
	v_pk_mul_f32 v[164:165], v[70:71], v[80:81] op_sel_hi:[1,0]
	v_pk_mul_f32 v[174:175], v[76:77], v[80:81] op_sel_hi:[1,0]
	v_pk_mul_f32 v[170:171], v[72:73], v[80:81] op_sel_hi:[1,0]
	v_max_f32_e32 v72, v172, v173
	v_max_f32_e32 v73, v166, v167
	v_pk_mul_f32 v[168:169], v[68:69], v[80:81] op_sel_hi:[1,0]
	v_max_f32_e32 v68, v164, v165
	v_pk_mul_f32 v[74:75], v[66:67], v[80:81] op_sel_hi:[1,0]
	v_max3_f32 v72, v174, v175, v72
	v_max3_f32 v73, v170, v171, v73
	v_max3_f32 v70, v168, v169, v68
	v_pk_mul_f32 v[68:69], v[64:65], v[80:81] op_sel_hi:[1,0]
	v_max_f32_e32 v64, v74, v75
	v_max3_f32 v72, v72, s34, v73
	v_max3_f32 v64, v68, v69, v64
	v_max3_f32 v64, v72, v70, v64
	v_mov_b32_e32 v65, v64
	s_nop 1
	v_permlane16_swap_b32_e32 v64, v65
	v_max_f32_e32 v65, v65, v65
	v_max_f32_e32 v64, v64, v64
	v_max_f32_e32 v64, v64, v65
	v_mov_b32_e32 v65, v64
	s_nop 1
	v_permlane32_swap_b32_e32 v64, v65
	s_and_saveexec_b64 s[22:23], s[4:5]
	v_max_f32_e32 v64, v64, v64
	v_max_f32_e32 v65, v65, v65
	v_max_f32_e32 v64, v64, v65
	ds_write_b32 v202, v64 offset:768
	s_or_b64 exec, exec, s[22:23]
	s_waitcnt lgkmcnt(5)
	v_mov_b32_e32 v64, v226
	v_mov_b32_e32 v65, v227
	v_mov_b32_e32 v66, v228
	v_mov_b32_e32 v67, v229
	ds_read_b128 v[226:229], v209
	v_mov_b32_e32 v70, v65
	v_mov_b32_e32 v71, v66
	v_mov_b32_e32 v65, v67
	v_pk_add_f32 v[64:65], v[70:71], v[64:65]
	s_nop 0
	v_add_f32_e32 v64, v64, v65
	v_fmamk_f32 v64, v64, 0x3a800000, v194
	v_mul_f32_e32 v65, 0x4b800000, v64
	v_cmp_gt_f32_e32 vcc, s64, v64
	s_nop 1
	v_cndmask_b32_e32 v64, v64, v65, vcc
	v_rsq_f32_e32 v64, v64
	s_nop 0
	v_mul_f32_e32 v65, 0x45800000, v64
	v_cndmask_b32_e32 v64, v64, v65, vcc
	v_pk_mul_f32 v[72:73], v[62:63], v[64:65] op_sel_hi:[1,0]
	v_pk_mul_f32 v[70:71], v[58:59], v[64:65] op_sel_hi:[1,0]
	v_pk_mul_f32 v[60:61], v[60:61], v[64:65] op_sel_hi:[1,0]
	v_pk_mul_f32 v[66:67], v[56:57], v[64:65] op_sel_hi:[1,0]
	v_max_f32_e32 v56, v72, v73
	v_max_f32_e32 v57, v70, v71
	v_pk_mul_f32 v[76:77], v[54:55], v[64:65] op_sel_hi:[1,0]
	v_pk_mul_f32 v[80:81], v[50:51], v[64:65] op_sel_hi:[1,0]
	v_max3_f32 v56, v60, v61, v56
	v_max3_f32 v57, v66, v67, v57
	v_pk_mul_f32 v[162:163], v[52:53], v[64:65] op_sel_hi:[1,0]
	v_max_f32_e32 v52, v76, v77
	v_pk_mul_f32 v[78:79], v[48:49], v[64:65] op_sel_hi:[1,0]
	v_max_f32_e32 v48, v80, v81
	v_max3_f32 v56, v56, s34, v57
	v_max3_f32 v52, v162, v163, v52
	v_max3_f32 v48, v78, v79, v48
	v_max3_f32 v48, v56, v52, v48
	v_mov_b32_e32 v49, v48
	s_nop 1
	v_permlane16_swap_b32_e32 v48, v49
	v_max_f32_e32 v49, v49, v49
	v_max_f32_e32 v48, v48, v48
	v_max_f32_e32 v48, v48, v49
	v_mov_b32_e32 v49, v48
	s_nop 1
	v_permlane32_swap_b32_e32 v48, v49
	s_and_saveexec_b64 s[22:23], s[4:5]
	v_max_f32_e32 v48, v48, v48
	v_max_f32_e32 v49, v49, v49
	v_max_f32_e32 v48, v48, v49
	ds_write_b32 v202, v48 offset:2048
	s_or_b64 exec, exec, s[22:23]
	s_waitcnt lgkmcnt(5)
	v_mov_b32_e32 v48, v230
	v_mov_b32_e32 v49, v231
	v_mov_b32_e32 v50, v232
	v_mov_b32_e32 v51, v233
	v_mov_b32_e32 v52, v49
	v_mov_b32_e32 v53, v50
	v_mov_b32_e32 v49, v51
	v_pk_add_f32 v[48:49], v[52:53], v[48:49]
	s_nop 0
	v_add_f32_e32 v48, v48, v49
	v_fmamk_f32 v48, v48, 0x3a800000, v194
	v_mul_f32_e32 v49, 0x4b800000, v48
	v_cmp_gt_f32_e32 vcc, s64, v48
	s_nop 1
	v_cndmask_b32_e32 v48, v48, v49, vcc
	v_rsq_f32_e32 v48, v48
	s_nop 0
	v_mul_f32_e32 v49, 0x45800000, v48
	v_cndmask_b32_e32 v48, v48, v49, vcc
	v_pk_mul_f32 v[158:159], v[46:47], v[48:49] op_sel_hi:[1,0]
	v_pk_mul_f32 v[152:153], v[42:43], v[48:49] op_sel_hi:[1,0]
	v_pk_mul_f32 v[160:161], v[44:45], v[48:49] op_sel_hi:[1,0]
	v_pk_mul_f32 v[156:157], v[40:41], v[48:49] op_sel_hi:[1,0]
	v_max_f32_e32 v40, v158, v159
	v_max_f32_e32 v41, v152, v153
	v_pk_mul_f32 v[150:151], v[38:39], v[48:49] op_sel_hi:[1,0]
	v_pk_mul_f32 v[42:43], v[34:35], v[48:49] op_sel_hi:[1,0]
	v_max3_f32 v40, v160, v161, v40
	v_max3_f32 v41, v156, v157, v41
	v_pk_mul_f32 v[154:155], v[36:37], v[48:49] op_sel_hi:[1,0]
	v_max_f32_e32 v36, v150, v151
	v_pk_mul_f32 v[34:35], v[32:33], v[48:49] op_sel_hi:[1,0]
	v_max_f32_e32 v32, v42, v43
	v_max3_f32 v40, v40, s34, v41
	v_max3_f32 v36, v154, v155, v36
	v_max3_f32 v32, v34, v35, v32
	v_max3_f32 v32, v40, v36, v32
	v_mov_b32_e32 v33, v32
	s_nop 1
	v_permlane16_swap_b32_e32 v32, v33
	v_max_f32_e32 v33, v33, v33
	v_max_f32_e32 v32, v32, v32
	v_max_f32_e32 v32, v32, v33
	v_mov_b32_e32 v33, v32
	s_nop 1
	v_permlane32_swap_b32_e32 v32, v33
	s_and_saveexec_b64 s[22:23], s[4:5]
	v_max_f32_e32 v32, v32, v32
	v_max_f32_e32 v33, v33, v33
	v_max_f32_e32 v32, v32, v33
	ds_write_b32 v202, v32 offset:2304
	s_or_b64 exec, exec, s[22:23]
	s_waitcnt lgkmcnt(4)
; #define PG8_LAS __attribute__((address_space(3)))
;     __device__ __forceinline__ void operator()(f32x4 (&acc)[2][2][4][2], const Unit& u, int wr, int wc, int fr, int fq) const {
;     ...
;             for (int m = 0; m < 4; ++m) { float t = -3.0e38f;
;                 const f32x4 s4 = *(PG8_LAS const f32x4*)(ss + (ai * HALF + wr * 64 + m * 16 + fr) * 4);
;                 const float rs = rsqrtf(((s4[0] + s4[1]) + (s4[2] + s4[3])) * (1.f / D) + 1e-6f);
; #pragma unroll
;                 for (int bj = 0; bj < 2; ++bj)
; #pragma unroll
;                     for (int n = 0; n < 2; ++n) { acc[ai][bj][m][n] = acc[ai][bj][m][n] * rs; const f32x4 v = acc[ai][bj][m][n]; t = fmaxf(t, fmaxf(fmaxf(v[0], v[1]), fmaxf(v[2], v[3]))); }
;                 t = rows_max4(t);
;                 if (fq == 0) smax[(ai * HALF + wr * 64 + m * 16 + fr) * 4 + wc] = t; }
;         asm volatile("s_waitcnt lgkmcnt(0)" ::: "memory"); __builtin_amdgcn_s_barrier(); asm volatile("" ::: "memory");
; #pragma unroll
;         for (int ai = 0; ai < 2; ++ai)
; #pragma unroll
;             for (int m = 0; m < 4; ++m) { const f32x4 q = *(const PG8_LAS f32x4*)(smax + (ai * HALF + wr * 64 + m * 16 + fr) * 4);
;                 const float mm = fmaxf(fmaxf(q[0], q[1]), fmaxf(q[2], q[3])) * SC; float s = 0.f;
; #pragma unroll
;                 for (int bj = 0; bj < 2; ++bj)
; #pragma unroll
;                     for (int n = 0; n < 2; ++n)
; #pragma unroll
;                         for (int e = 0; e < 4; ++e) { const float p = __builtin_amdgcn_exp2f(acc[ai][bj][m][n][e] * SC - mm); acc[ai][bj][m][n][e] = p; s += p; }
;                 s = rows_sum4(s);
;                 if (fq == 0) ssum[(ai * HALF + wr * 64 + m * 16 + fr) * 4 + wc] = s; }
	v_mov_b32_e32 v36, v222
	v_mov_b32_e32 v37, v223
	v_mov_b32_e32 v38, v224
	v_mov_b32_e32 v39, v225
	v_mov_b32_e32 v32, v37
	v_mov_b32_e32 v33, v38
	v_mov_b32_e32 v37, v39
	v_pk_add_f32 v[32:33], v[32:33], v[36:37]
	s_nop 0
	v_add_f32_e32 v32, v32, v33
	v_fmamk_f32 v32, v32, 0x3a800000, v194
	v_mul_f32_e32 v33, 0x4b800000, v32
	v_cmp_gt_f32_e32 vcc, s64, v32
	s_nop 1
	v_cndmask_b32_e32 v32, v32, v33, vcc
	v_rsq_f32_e32 v32, v32
	s_nop 0
	v_mul_f32_e32 v33, 0x45800000, v32
	v_cndmask_b32_e32 v36, v32, v33, vcc
	v_pk_mul_f32 v[40:41], v[30:31], v[36:37] op_sel_hi:[1,0]
	v_pk_mul_f32 v[38:39], v[26:27], v[36:37] op_sel_hi:[1,0]
	v_pk_mul_f32 v[28:29], v[28:29], v[36:37] op_sel_hi:[1,0]
	v_pk_mul_f32 v[32:33], v[24:25], v[36:37] op_sel_hi:[1,0]
	v_max_f32_e32 v24, v40, v41
	v_max_f32_e32 v25, v38, v39
	v_pk_mul_f32 v[44:45], v[22:23], v[36:37] op_sel_hi:[1,0]
	v_pk_mul_f32 v[48:49], v[18:19], v[36:37] op_sel_hi:[1,0]
	v_max3_f32 v24, v28, v29, v24
	v_max3_f32 v25, v32, v33, v25
	v_pk_mul_f32 v[148:149], v[20:21], v[36:37] op_sel_hi:[1,0]
	v_max_f32_e32 v20, v44, v45
	v_pk_mul_f32 v[46:47], v[16:17], v[36:37] op_sel_hi:[1,0]
	v_max_f32_e32 v16, v48, v49
	v_max3_f32 v24, v24, s34, v25
	v_max3_f32 v20, v148, v149, v20
	v_max3_f32 v16, v46, v47, v16
	v_max3_f32 v16, v24, v20, v16
	v_mov_b32_e32 v17, v16
	s_nop 1
	v_permlane16_swap_b32_e32 v16, v17
	v_max_f32_e32 v17, v17, v17
	v_max_f32_e32 v16, v16, v16
	v_max_f32_e32 v16, v16, v17
	v_mov_b32_e32 v17, v16
	s_nop 1
	v_permlane32_swap_b32_e32 v16, v17
	s_and_saveexec_b64 s[22:23], s[4:5]
	v_max_f32_e32 v16, v16, v16
	v_max_f32_e32 v17, v17, v17
	v_max_f32_e32 v16, v16, v17
	ds_write_b32 v202, v16 offset:2560
	s_or_b64 exec, exec, s[22:23]
	s_waitcnt lgkmcnt(3)
	v_mov_b32_e32 v16, v226
	v_mov_b32_e32 v17, v227
	v_mov_b32_e32 v18, v228
	v_mov_b32_e32 v19, v229
	v_mov_b32_e32 v20, v17
	v_mov_b32_e32 v21, v18
	v_mov_b32_e32 v17, v19
	v_pk_add_f32 v[16:17], v[20:21], v[16:17]
	s_nop 0
	v_add_f32_e32 v16, v16, v17
	v_fmamk_f32 v16, v16, 0x3a800000, v194
	v_mul_f32_e32 v17, 0x4b800000, v16
	v_cmp_gt_f32_e32 vcc, s64, v16
	s_nop 1
	v_cndmask_b32_e32 v16, v16, v17, vcc
	v_rsq_f32_e32 v16, v16
	s_nop 0
	v_mul_f32_e32 v17, 0x45800000, v16
	v_cndmask_b32_e32 v18, v16, v17, vcc
	v_pk_mul_f32 v[116:117], v[14:15], v[18:19] op_sel_hi:[1,0]
	v_pk_mul_f32 v[146:147], v[12:13], v[18:19] op_sel_hi:[1,0]
	v_pk_mul_f32 v[12:13], v[10:11], v[18:19] op_sel_hi:[1,0]
	v_pk_mul_f32 v[114:115], v[8:9], v[18:19] op_sel_hi:[1,0]
	v_max_f32_e32 v8, v116, v117
	v_max_f32_e32 v9, v12, v13
	v_max3_f32 v8, v146, v147, v8
	v_max3_f32 v9, v114, v115, v9
	v_max3_f32 v19, v8, s34, v9
	v_pk_mul_f32 v[10:11], v[6:7], v[18:19] op_sel_hi:[1,0]
	v_pk_mul_f32 v[14:15], v[2:3], v[18:19] op_sel_hi:[1,0]
	v_pk_mul_f32 v[16:17], v[4:5], v[18:19] op_sel_hi:[1,0]
	v_max_f32_e32 v4, v10, v11
	v_pk_mul_f32 v[8:9], v[0:1], v[18:19] op_sel_hi:[1,0]
	v_max_f32_e32 v0, v14, v15
	v_max3_f32 v4, v16, v17, v4
	v_max3_f32 v0, v8, v9, v0
	v_max3_f32 v0, v19, v4, v0
	v_mov_b32_e32 v1, v0
	s_nop 1
	v_permlane16_swap_b32_e32 v0, v1
	v_max_f32_e32 v1, v1, v1
	v_max_f32_e32 v0, v0, v0
	v_max_f32_e32 v0, v0, v1
	v_mov_b32_e32 v1, v0
	s_nop 1
	v_permlane32_swap_b32_e32 v0, v1
	s_and_saveexec_b64 s[22:23], s[4:5]
	v_max_f32_e32 v0, v0, v0
	v_max_f32_e32 v1, v1, v1
	v_max_f32_e32 v0, v0, v1
	ds_write_b32 v202, v0 offset:2816
	s_or_b64 exec, exec, s[22:23]
	s_waitcnt lgkmcnt(0)
	s_barrier
	ds_read_b128 v[222:225], v210
	ds_read_b128 v[226:229], v212
	ds_read_b128 v[230:233], v213
	v_mov_b32_e32 v4, v145
	s_waitcnt lgkmcnt(2)
	v_mov_b32_e32 v0, v222
	v_mov_b32_e32 v1, v223
	v_mov_b32_e32 v2, v224
	v_mov_b32_e32 v3, v225
	ds_read_b128 v[222:225], v214
	v_max_f32_e32 v3, v3, v3
	v_max_f32_e32 v2, v2, v2
	v_max_f32_e32 v2, v2, v3
	v_max3_f32 v5, v0, v1, v2
	v_pk_mul_f32 v[0:1], v[4:5], s[70:71] op_sel_hi:[1,0]
	s_nop 0
	v_fma_f32 v2, v192, s70, -v1
	v_exp_f32_e32 v118, v2
	v_fma_f32 v2, v193, s70, -v1
	v_exp_f32_e32 v119, v2
	v_fma_f32 v2, v190, s70, -v1
	v_exp_f32_e32 v120, v2
	v_fma_f32 v2, v191, s70, -v1
	v_exp_f32_e32 v121, v2
	v_fma_f32 v3, v122, s70, -v1
	v_add_f32_e32 v2, 0, v118
	v_exp_f32_e32 v122, v3
	v_fma_f32 v3, v123, s70, -v1
	v_add_f32_e32 v2, v119, v2
	v_exp_f32_e32 v123, v3
	v_fma_f32 v3, v124, s70, -v1
	v_add_f32_e32 v2, v120, v2
	v_exp_f32_e32 v124, v3
	v_fma_f32 v3, v125, s70, -v1
	v_add_f32_e32 v2, v121, v2
	v_exp_f32_e32 v125, v3
	v_fma_f32 v3, v126, s70, -v1
	v_add_f32_e32 v2, v122, v2
	v_exp_f32_e32 v126, v3
	v_fma_f32 v3, v127, s70, -v1
	v_add_f32_e32 v2, v123, v2
	v_exp_f32_e32 v127, v3
	v_fma_f32 v3, v140, s70, -v1
	v_add_f32_e32 v2, v124, v2
	v_exp_f32_e32 v140, v3
	v_fma_f32 v3, v141, s70, -v1
	v_add_f32_e32 v2, v125, v2
	v_exp_f32_e32 v141, v3
	v_fma_f32 v3, v142, s70, -v1
	v_add_f32_e32 v2, v126, v2
	v_exp_f32_e32 v142, v3
	v_fma_f32 v3, v143, s70, -v1
	v_add_f32_e32 v2, v127, v2
	v_exp_f32_e32 v143, v3
	v_fma_f32 v3, v144, s70, -v1
	v_add_f32_e32 v2, v140, v2
	v_exp_f32_e32 v144, v3
	v_sub_f32_e32 v0, v0, v1
	v_add_f32_e32 v2, v141, v2
	v_exp_f32_e32 v145, v0
	v_add_f32_e32 v0, v142, v2
	v_add_f32_e32 v0, v143, v0
	v_add_f32_e32 v0, v144, v0
	v_add_f32_e32 v0, v145, v0
	v_mov_b32_e32 v1, v0
	s_nop 1
	v_permlane16_swap_b32_e32 v0, v1
	v_add_f32_e32 v0, v0, v1
	v_mov_b32_e32 v1, v0
	s_nop 1
	v_permlane32_swap_b32_e32 v0, v1
	s_and_saveexec_b64 s[22:23], s[4:5]
	v_add_f32_e32 v0, v0, v1
	ds_write_b32 v211, v0
	s_or_b64 exec, exec, s[22:23]
	v_mov_b32_e32 v4, v107
	s_waitcnt lgkmcnt(3)
; #define PG8_LAS __attribute__((address_space(3)))
;     __device__ __forceinline__ void operator()(f32x4 (&acc)[2][2][4][2], const Unit& u, int wr, int wc, int fr, int fq) const {
;     ...
; #pragma unroll
;         for (int ai = 0; ai < 2; ++ai)
; #pragma unroll
;             for (int m = 0; m < 4; ++m) { const f32x4 q = *(const PG8_LAS f32x4*)(smax + (ai * HALF + wr * 64 + m * 16 + fr) * 4);
;                 const float mm = fmaxf(fmaxf(q[0], q[1]), fmaxf(q[2], q[3])) * SC; float s = 0.f;
; #pragma unroll
;                 for (int bj = 0; bj < 2; ++bj)
; #pragma unroll
;                     for (int n = 0; n < 2; ++n)
; #pragma unroll
;                         for (int e = 0; e < 4; ++e) { const float p = __builtin_amdgcn_exp2f(acc[ai][bj][m][n][e] * SC - mm); acc[ai][bj][m][n][e] = p; s += p; }
;                 s = rows_sum4(s);
;                 if (fq == 0) ssum[(ai * HALF + wr * 64 + m * 16 + fr) * 4 + wc] = s; }
	v_mov_b32_e32 v0, v226
	v_mov_b32_e32 v1, v227
	v_mov_b32_e32 v2, v228
	v_mov_b32_e32 v3, v229
	ds_read_b128 v[226:229], v215
	v_max_f32_e32 v3, v3, v3
	v_max_f32_e32 v2, v2, v2
	v_max_f32_e32 v2, v2, v3
	v_max3_f32 v5, v0, v1, v2
	v_pk_mul_f32 v[0:1], v[4:5], s[70:71] op_sel_hi:[1,0]
	s_nop 0
	v_fma_f32 v2, v188, s70, -v1
	v_fma_f32 v3, v189, s70, -v1
	v_exp_f32_e32 v82, v2
	v_exp_f32_e32 v83, v3
	v_fma_f32 v2, v186, s70, -v1
	v_exp_f32_e32 v90, v2
	v_fma_f32 v2, v187, s70, -v1
	v_exp_f32_e32 v91, v2
	v_fma_f32 v3, v184, s70, -v1
	v_add_f32_e32 v2, 0, v82
	v_exp_f32_e32 v88, v3
	v_fma_f32 v3, v185, s70, -v1
	v_add_f32_e32 v2, v83, v2
	v_exp_f32_e32 v89, v3
	v_fma_f32 v3, v180, s70, -v1
	v_add_f32_e32 v2, v90, v2
	v_exp_f32_e32 v98, v3
	v_fma_f32 v3, v181, s70, -v1
	v_add_f32_e32 v2, v91, v2
	v_exp_f32_e32 v99, v3
	v_fma_f32 v3, v182, s70, -v1
	v_add_f32_e32 v2, v88, v2
	v_exp_f32_e32 v86, v3
	v_fma_f32 v3, v183, s70, -v1
	v_add_f32_e32 v2, v89, v2
	v_exp_f32_e32 v87, v3
	v_fma_f32 v3, v178, s70, -v1
	v_add_f32_e32 v2, v98, v2
	v_exp_f32_e32 v96, v3
	v_fma_f32 v3, v179, s70, -v1
	v_add_f32_e32 v2, v99, v2
	v_exp_f32_e32 v97, v3
	v_fma_f32 v3, v100, s70, -v1
	v_add_f32_e32 v2, v86, v2
	v_exp_f32_e32 v100, v3
	v_fma_f32 v3, v101, s70, -v1
	v_add_f32_e32 v2, v87, v2
	v_exp_f32_e32 v101, v3
	v_fma_f32 v3, v106, s70, -v1
	v_add_f32_e32 v2, v96, v2
	v_exp_f32_e32 v106, v3
	v_sub_f32_e32 v0, v0, v1
	v_add_f32_e32 v2, v97, v2
	v_exp_f32_e32 v107, v0
	v_add_f32_e32 v0, v100, v2
	v_add_f32_e32 v0, v101, v0
	v_add_f32_e32 v0, v106, v0
	v_add_f32_e32 v0, v107, v0
	v_mov_b32_e32 v1, v0
	s_nop 1
	v_permlane16_swap_b32_e32 v0, v1
	v_add_f32_e32 v0, v0, v1
	v_mov_b32_e32 v1, v0
	s_nop 1
	v_permlane32_swap_b32_e32 v0, v1
	s_and_saveexec_b64 s[22:23], s[4:5]
	v_add_f32_e32 v0, v0, v1
	ds_write_b32 v211, v0 offset:256
	s_or_b64 exec, exec, s[22:23]
	v_mov_b32_e32 v4, v113
	s_waitcnt lgkmcnt(4)
	v_mov_b32_e32 v0, v230
	v_mov_b32_e32 v1, v231
	v_mov_b32_e32 v2, v232
	v_mov_b32_e32 v3, v233
	ds_read_b128 v[230:233], v216
	v_max_f32_e32 v3, v3, v3
	v_max_f32_e32 v2, v2, v2
	v_max_f32_e32 v2, v2, v3
	v_max3_f32 v5, v0, v1, v2
	v_pk_mul_f32 v[0:1], v[4:5], s[70:71] op_sel_hi:[1,0]
	s_nop 0
	v_fma_f32 v2, v92, s70, -v1
	v_fma_f32 v3, v93, s70, -v1
	v_exp_f32_e32 v84, v2
	v_exp_f32_e32 v85, v3
	v_fma_f32 v2, v176, s70, -v1
	v_exp_f32_e32 v92, v2
	v_fma_f32 v2, v177, s70, -v1
	v_exp_f32_e32 v93, v2
	v_fma_f32 v3, v94, s70, -v1
	v_add_f32_e32 v2, 0, v84
	v_exp_f32_e32 v94, v3
	v_fma_f32 v3, v95, s70, -v1
	v_add_f32_e32 v2, v85, v2
	v_exp_f32_e32 v95, v3
	v_fma_f32 v3, v102, s70, -v1
	v_add_f32_e32 v2, v92, v2
	v_exp_f32_e32 v102, v3
	v_fma_f32 v3, v103, s70, -v1
	v_add_f32_e32 v2, v93, v2
	v_exp_f32_e32 v103, v3
	v_fma_f32 v3, v104, s70, -v1
	v_add_f32_e32 v2, v94, v2
	v_exp_f32_e32 v104, v3
	v_fma_f32 v3, v105, s70, -v1
	v_add_f32_e32 v2, v95, v2
	v_exp_f32_e32 v105, v3
	v_fma_f32 v3, v108, s70, -v1
	v_add_f32_e32 v2, v102, v2
	v_exp_f32_e32 v108, v3
	v_fma_f32 v3, v109, s70, -v1
	v_add_f32_e32 v2, v103, v2
	v_exp_f32_e32 v109, v3
	v_fma_f32 v3, v110, s70, -v1
	v_add_f32_e32 v2, v104, v2
	v_exp_f32_e32 v110, v3
	v_fma_f32 v3, v111, s70, -v1
	v_add_f32_e32 v2, v105, v2
	v_exp_f32_e32 v111, v3
	v_fma_f32 v3, v112, s70, -v1
	v_add_f32_e32 v2, v108, v2
	v_exp_f32_e32 v112, v3
	v_sub_f32_e32 v0, v0, v1
	v_add_f32_e32 v2, v109, v2
	v_exp_f32_e32 v113, v0
	v_add_f32_e32 v0, v110, v2
	v_add_f32_e32 v0, v111, v0
	v_add_f32_e32 v0, v112, v0
	v_add_f32_e32 v0, v113, v0
	v_mov_b32_e32 v1, v0
	s_nop 1
	v_permlane16_swap_b32_e32 v0, v1
	v_add_f32_e32 v0, v0, v1
	v_mov_b32_e32 v1, v0
	s_nop 1
	v_permlane32_swap_b32_e32 v0, v1
	s_and_saveexec_b64 s[22:23], s[4:5]
	v_add_f32_e32 v0, v0, v1
	ds_write_b32 v211, v0 offset:512
	s_or_b64 exec, exec, s[22:23]
	v_mov_b32_e32 v4, v75
	s_waitcnt lgkmcnt(5)
	v_mov_b32_e32 v0, v222
	v_mov_b32_e32 v1, v223
	v_mov_b32_e32 v2, v224
	v_mov_b32_e32 v3, v225
	ds_read_b128 v[222:225], v217
	v_max_f32_e32 v3, v3, v3
	v_max_f32_e32 v2, v2, v2
	v_max_f32_e32 v2, v2, v3
	v_max3_f32 v5, v0, v1, v2
	v_pk_mul_f32 v[0:1], v[4:5], s[70:71] op_sel_hi:[1,0]
	s_nop 0
	v_fma_f32 v2, v174, s70, -v1
	v_fma_f32 v3, v175, s70, -v1
	v_exp_f32_e32 v50, v2
	v_exp_f32_e32 v51, v3
	v_fma_f32 v2, v172, s70, -v1
	v_exp_f32_e32 v56, v2
	v_fma_f32 v2, v173, s70, -v1
	v_exp_f32_e32 v57, v2
	v_fma_f32 v3, v170, s70, -v1
	v_add_f32_e32 v2, 0, v50
	v_exp_f32_e32 v54, v3
	v_fma_f32 v3, v171, s70, -v1
	v_add_f32_e32 v2, v51, v2
	v_exp_f32_e32 v55, v3
	v_fma_f32 v3, v166, s70, -v1
	v_add_f32_e32 v2, v56, v2
	v_exp_f32_e32 v64, v3
	v_fma_f32 v3, v167, s70, -v1
	v_add_f32_e32 v2, v57, v2
	v_exp_f32_e32 v65, v3
	v_fma_f32 v3, v168, s70, -v1
	v_add_f32_e32 v2, v54, v2
	v_exp_f32_e32 v52, v3
	v_fma_f32 v3, v169, s70, -v1
	v_add_f32_e32 v2, v55, v2
	v_exp_f32_e32 v53, v3
	v_fma_f32 v3, v164, s70, -v1
	v_add_f32_e32 v2, v64, v2
	v_exp_f32_e32 v62, v3
	v_fma_f32 v3, v165, s70, -v1
	v_add_f32_e32 v2, v65, v2
	v_exp_f32_e32 v63, v3
	v_fma_f32 v3, v68, s70, -v1
	v_add_f32_e32 v2, v52, v2
	v_exp_f32_e32 v68, v3
	v_fma_f32 v3, v69, s70, -v1
	v_add_f32_e32 v2, v53, v2
	v_exp_f32_e32 v69, v3
	v_fma_f32 v3, v74, s70, -v1
	v_add_f32_e32 v2, v62, v2
	v_exp_f32_e32 v74, v3
	v_sub_f32_e32 v0, v0, v1
	v_add_f32_e32 v2, v63, v2
	v_exp_f32_e32 v75, v0
	v_add_f32_e32 v0, v68, v2
	v_add_f32_e32 v0, v69, v0
	v_add_f32_e32 v0, v74, v0
	v_add_f32_e32 v0, v75, v0
	v_mov_b32_e32 v1, v0
	s_nop 1
	v_permlane16_swap_b32_e32 v0, v1
	v_add_f32_e32 v0, v0, v1
	v_mov_b32_e32 v1, v0
	s_nop 1
	v_permlane32_swap_b32_e32 v0, v1
	s_and_saveexec_b64 s[22:23], s[4:5]
	v_add_f32_e32 v0, v0, v1
	ds_write_b32 v211, v0 offset:768
	s_or_b64 exec, exec, s[22:23]
	v_mov_b32_e32 v4, v81
	s_waitcnt lgkmcnt(5)
; #define PG8_LAS __attribute__((address_space(3)))
;     __device__ __forceinline__ void operator()(f32x4 (&acc)[2][2][4][2], const Unit& u, int wr, int wc, int fr, int fq) const {
;     ...
; #pragma unroll
;         for (int ai = 0; ai < 2; ++ai)
; #pragma unroll
;             for (int m = 0; m < 4; ++m) { const f32x4 q = *(const PG8_LAS f32x4*)(smax + (ai * HALF + wr * 64 + m * 16 + fr) * 4);
;                 const float mm = fmaxf(fmaxf(q[0], q[1]), fmaxf(q[2], q[3])) * SC; float s = 0.f;
; #pragma unroll
;                 for (int bj = 0; bj < 2; ++bj)
; #pragma unroll
;                     for (int n = 0; n < 2; ++n)
; #pragma unroll
;                         for (int e = 0; e < 4; ++e) { const float p = __builtin_amdgcn_exp2f(acc[ai][bj][m][n][e] * SC - mm); acc[ai][bj][m][n][e] = p; s += p; }
;                 s = rows_sum4(s);
;                 if (fq == 0) ssum[(ai * HALF + wr * 64 + m * 16 + fr) * 4 + wc] = s; }
	v_mov_b32_e32 v0, v226
	v_mov_b32_e32 v1, v227
	v_mov_b32_e32 v2, v228
	v_mov_b32_e32 v3, v229
	ds_read_b128 v[226:229], v218
	v_max_f32_e32 v3, v3, v3
	v_max_f32_e32 v2, v2, v2
	v_max_f32_e32 v2, v2, v3
	v_max3_f32 v5, v0, v1, v2
	v_pk_mul_f32 v[0:1], v[4:5], s[70:71] op_sel_hi:[1,0]
	s_nop 0
	v_fma_f32 v2, v60, s70, -v1
	v_fma_f32 v3, v61, s70, -v1
	v_exp_f32_e32 v58, v2
	v_exp_f32_e32 v59, v3
	v_fma_f32 v2, v72, s70, -v1
	v_exp_f32_e32 v60, v2
	v_fma_f32 v2, v73, s70, -v1
	v_exp_f32_e32 v61, v2
	v_fma_f32 v3, v66, s70, -v1
	v_add_f32_e32 v2, 0, v58
	v_exp_f32_e32 v66, v3
	v_fma_f32 v3, v67, s70, -v1
	v_add_f32_e32 v2, v59, v2
	v_exp_f32_e32 v67, v3
	v_fma_f32 v3, v70, s70, -v1
	v_add_f32_e32 v2, v60, v2
	v_exp_f32_e32 v72, v3
	v_fma_f32 v3, v71, s70, -v1
	v_add_f32_e32 v2, v61, v2
	v_exp_f32_e32 v73, v3
	v_fma_f32 v3, v162, s70, -v1
	v_add_f32_e32 v2, v66, v2
	v_exp_f32_e32 v70, v3
	v_fma_f32 v3, v163, s70, -v1
	v_add_f32_e32 v2, v67, v2
	v_exp_f32_e32 v71, v3
	v_fma_f32 v3, v76, s70, -v1
	v_add_f32_e32 v2, v72, v2
	v_exp_f32_e32 v76, v3
	v_fma_f32 v3, v77, s70, -v1
	v_add_f32_e32 v2, v73, v2
	v_exp_f32_e32 v77, v3
	v_fma_f32 v3, v78, s70, -v1
	v_add_f32_e32 v2, v70, v2
	v_exp_f32_e32 v78, v3
	v_fma_f32 v3, v79, s70, -v1
	v_add_f32_e32 v2, v71, v2
	v_exp_f32_e32 v79, v3
	v_fma_f32 v3, v80, s70, -v1
	v_add_f32_e32 v2, v76, v2
	v_exp_f32_e32 v80, v3
	v_sub_f32_e32 v0, v0, v1
	v_add_f32_e32 v2, v77, v2
	v_exp_f32_e32 v81, v0
	v_add_f32_e32 v0, v78, v2
	v_add_f32_e32 v0, v79, v0
	v_add_f32_e32 v0, v80, v0
	v_add_f32_e32 v0, v81, v0
	v_mov_b32_e32 v1, v0
	s_nop 1
	v_permlane16_swap_b32_e32 v0, v1
	v_add_f32_e32 v0, v0, v1
	v_mov_b32_e32 v1, v0
	s_nop 1
	v_permlane32_swap_b32_e32 v0, v1
	s_and_saveexec_b64 s[22:23], s[4:5]
	v_add_f32_e32 v0, v0, v1
	ds_write_b32 v211, v0 offset:2048
	s_or_b64 exec, exec, s[22:23]
	v_mov_b32_e32 v4, v43
	s_waitcnt lgkmcnt(5)
	v_mov_b32_e32 v0, v230
	v_mov_b32_e32 v1, v231
	v_mov_b32_e32 v2, v232
	v_mov_b32_e32 v3, v233
	v_max_f32_e32 v3, v3, v3
	v_max_f32_e32 v2, v2, v2
	v_max_f32_e32 v2, v2, v3
	v_max3_f32 v5, v0, v1, v2
	v_pk_mul_f32 v[0:1], v[4:5], s[70:71] op_sel_hi:[1,0]
	s_nop 0
	v_fma_f32 v2, v160, s70, -v1
	v_fma_f32 v3, v161, s70, -v1
	v_exp_f32_e32 v18, v2
	v_exp_f32_e32 v19, v3
	v_fma_f32 v2, v158, s70, -v1
	v_exp_f32_e32 v26, v2
	v_fma_f32 v2, v159, s70, -v1
	v_exp_f32_e32 v27, v2
	v_fma_f32 v3, v156, s70, -v1
	v_add_f32_e32 v2, 0, v18
	v_exp_f32_e32 v24, v3
	v_fma_f32 v3, v157, s70, -v1
	v_add_f32_e32 v2, v19, v2
	v_exp_f32_e32 v25, v3
	v_fma_f32 v3, v152, s70, -v1
	v_add_f32_e32 v2, v26, v2
	v_exp_f32_e32 v36, v3
	v_fma_f32 v3, v153, s70, -v1
	v_add_f32_e32 v2, v27, v2
	v_exp_f32_e32 v37, v3
	v_fma_f32 v3, v154, s70, -v1
	v_add_f32_e32 v2, v24, v2
	v_exp_f32_e32 v20, v3
	v_fma_f32 v3, v155, s70, -v1
	v_add_f32_e32 v2, v25, v2
	v_exp_f32_e32 v21, v3
	v_fma_f32 v3, v150, s70, -v1
	v_add_f32_e32 v2, v36, v2
	v_exp_f32_e32 v30, v3
	v_fma_f32 v3, v151, s70, -v1
	v_add_f32_e32 v2, v37, v2
	v_exp_f32_e32 v31, v3
	v_fma_f32 v3, v34, s70, -v1
	v_add_f32_e32 v2, v20, v2
	v_exp_f32_e32 v34, v3
	v_fma_f32 v3, v35, s70, -v1
	v_add_f32_e32 v2, v21, v2
	v_exp_f32_e32 v35, v3
	v_fma_f32 v3, v42, s70, -v1
	v_add_f32_e32 v2, v30, v2
	v_exp_f32_e32 v42, v3
	v_sub_f32_e32 v0, v0, v1
	v_add_f32_e32 v2, v31, v2
	v_exp_f32_e32 v43, v0
	v_add_f32_e32 v0, v34, v2
	v_add_f32_e32 v0, v35, v0
	v_add_f32_e32 v0, v42, v0
	v_add_f32_e32 v0, v43, v0
	v_mov_b32_e32 v1, v0
	s_nop 1
	v_permlane16_swap_b32_e32 v0, v1
	v_add_f32_e32 v0, v0, v1
	v_mov_b32_e32 v1, v0
	s_nop 1
	v_permlane32_swap_b32_e32 v0, v1
	s_and_saveexec_b64 s[22:23], s[4:5]
	v_add_f32_e32 v0, v0, v1
	ds_write_b32 v211, v0 offset:2304
	s_or_b64 exec, exec, s[22:23]
	v_mov_b32_e32 v4, v49
	s_waitcnt lgkmcnt(4)
	v_mov_b32_e32 v0, v222
	v_mov_b32_e32 v1, v223
	v_mov_b32_e32 v2, v224
	v_mov_b32_e32 v3, v225
	v_max_f32_e32 v3, v3, v3
	v_max_f32_e32 v2, v2, v2
	v_max_f32_e32 v2, v2, v3
	v_max3_f32 v5, v0, v1, v2
	v_pk_mul_f32 v[0:1], v[4:5], s[70:71] op_sel_hi:[1,0]
	s_nop 0
	v_fma_f32 v2, v28, s70, -v1
	v_fma_f32 v3, v29, s70, -v1
	v_exp_f32_e32 v22, v2
	v_exp_f32_e32 v23, v3
	v_fma_f32 v2, v40, s70, -v1
	v_exp_f32_e32 v28, v2
	v_fma_f32 v2, v41, s70, -v1
	v_exp_f32_e32 v29, v2
	v_fma_f32 v3, v32, s70, -v1
	v_add_f32_e32 v2, 0, v22
	v_exp_f32_e32 v32, v3
	v_fma_f32 v3, v33, s70, -v1
	v_add_f32_e32 v2, v23, v2
	v_exp_f32_e32 v33, v3
	v_fma_f32 v3, v38, s70, -v1
	v_add_f32_e32 v2, v28, v2
	v_exp_f32_e32 v40, v3
	v_fma_f32 v3, v39, s70, -v1
	v_add_f32_e32 v2, v29, v2
	v_exp_f32_e32 v41, v3
	v_fma_f32 v3, v148, s70, -v1
	v_add_f32_e32 v2, v32, v2
	v_exp_f32_e32 v38, v3
	v_fma_f32 v3, v149, s70, -v1
	v_add_f32_e32 v2, v33, v2
	v_exp_f32_e32 v39, v3
	v_fma_f32 v3, v44, s70, -v1
	v_add_f32_e32 v2, v40, v2
	v_exp_f32_e32 v44, v3
	v_fma_f32 v3, v45, s70, -v1
	v_add_f32_e32 v2, v41, v2
	v_exp_f32_e32 v45, v3
	v_fma_f32 v3, v46, s70, -v1
	v_add_f32_e32 v2, v38, v2
	v_exp_f32_e32 v46, v3
	v_fma_f32 v3, v47, s70, -v1
	v_add_f32_e32 v2, v39, v2
	v_exp_f32_e32 v47, v3
	v_fma_f32 v3, v48, s70, -v1
	v_add_f32_e32 v2, v44, v2
	v_exp_f32_e32 v48, v3
	v_sub_f32_e32 v0, v0, v1
	v_add_f32_e32 v2, v45, v2
	v_exp_f32_e32 v49, v0
	v_add_f32_e32 v0, v46, v2
	v_add_f32_e32 v0, v47, v0
	v_add_f32_e32 v0, v48, v0
	v_add_f32_e32 v0, v49, v0
	v_mov_b32_e32 v1, v0
	s_nop 1
	v_permlane16_swap_b32_e32 v0, v1
	v_add_f32_e32 v0, v0, v1
	v_mov_b32_e32 v1, v0
	s_nop 1
	v_permlane32_swap_b32_e32 v0, v1
	s_and_saveexec_b64 s[22:23], s[4:5]
	v_add_f32_e32 v0, v0, v1
	ds_write_b32 v211, v0 offset:2560
	s_or_b64 exec, exec, s[22:23]
	v_mov_b32_e32 v4, v15
	s_waitcnt lgkmcnt(3)
; #define PG8_LAS __attribute__((address_space(3)))
; __device__ __forceinline__ unsigned cvt_pk_bf16(float lo, float hi) { const f32x2c v = {lo, hi}; const bf16x2c b = __builtin_convertvector(v, bf16x2c); return __builtin_bit_cast(unsigned, b); }
;     __device__ __forceinline__ void operator()(f32x4 (&acc)[2][2][4][2], const Unit& u, int wr, int wc, int fr, int fq) const {
;     ...
;             for (int m = 0; m < 4; ++m) { const f32x4 q = *(const PG8_LAS f32x4*)(smax + (ai * HALF + wr * 64 + m * 16 + fr) * 4);
;                 const float mm = fmaxf(fmaxf(q[0], q[1]), fmaxf(q[2], q[3])) * SC; float s = 0.f;
; #pragma unroll
;                 for (int bj = 0; bj < 2; ++bj)
; #pragma unroll
;                     for (int n = 0; n < 2; ++n)
; #pragma unroll
;                         for (int e = 0; e < 4; ++e) { const float p = __builtin_amdgcn_exp2f(acc[ai][bj][m][n][e] * SC - mm); acc[ai][bj][m][n][e] = p; s += p; }
;                 s = rows_sum4(s);
;                 if (fq == 0) ssum[(ai * HALF + wr * 64 + m * 16 + fr) * 4 + wc] = s; }
;         asm volatile("s_waitcnt lgkmcnt(0)" ::: "memory"); __builtin_amdgcn_s_barrier(); asm volatile("" ::: "memory");
;         const int row0 = u.pm * BM + wr * 64 + fr, col0 = u.pn * 256 + wc * 32 + 8 * fq;
; #pragma unroll
;         for (int ai = 0; ai < 2; ++ai)
; #pragma unroll
;             for (int m = 0; m < 4; ++m) { const f32x4 q = *(const PG8_LAS f32x4*)(ssum + (ai * HALF + wr * 64 + m * 16 + fr) * 4);
;                 const float iv = 1.f / ((q[0] + q[1]) + (q[2] + q[3]));
;                 bf16* rowp = P + (size_t)(row0 + ai * HALF + m * 16) * D + col0;
; #pragma unroll
;                 for (int bj = 0; bj < 2; ++bj) { const f32x4 v0 = acc[ai][bj][m][0] * iv, v1 = acc[ai][bj][m][1] * iv; u32x4 w;
;                     w.x = cvt_pk_bf16(v0[0], v0[1]); w.y = cvt_pk_bf16(v0[2], v0[3]); w.z = cvt_pk_bf16(v1[0], v1[1]); w.w = cvt_pk_bf16(v1[2], v1[3]);
;                     *(u32x4*)(rowp + bj * HALF) = w; } }
	v_mov_b32_e32 v0, v226
	v_mov_b32_e32 v1, v227
	v_mov_b32_e32 v2, v228
	v_mov_b32_e32 v3, v229
	v_max_f32_e32 v3, v3, v3
	v_max_f32_e32 v2, v2, v2
	v_max_f32_e32 v2, v2, v3
	v_max3_f32 v5, v0, v1, v2
	v_pk_mul_f32 v[148:149], v[4:5], s[70:71] op_sel_hi:[1,0]
	s_nop 0
	v_fma_f32 v0, v146, s70, -v149
	v_fma_f32 v1, v147, s70, -v149
	v_exp_f32_e32 v0, v0
	v_exp_f32_e32 v1, v1
	v_fma_f32 v2, v116, s70, -v149
	v_exp_f32_e32 v6, v2
	v_fma_f32 v2, v117, s70, -v149
	v_exp_f32_e32 v7, v2
	v_fma_f32 v3, v114, s70, -v149
	v_add_f32_e32 v2, 0, v0
	v_exp_f32_e32 v4, v3
	v_fma_f32 v3, v115, s70, -v149
	v_add_f32_e32 v2, v1, v2
	v_exp_f32_e32 v5, v3
	v_fma_f32 v3, v12, s70, -v149
	v_add_f32_e32 v2, v6, v2
	v_exp_f32_e32 v12, v3
	v_fma_f32 v3, v13, s70, -v149
	v_add_f32_e32 v2, v7, v2
	v_exp_f32_e32 v13, v3
	v_add_f32_e32 v2, v4, v2
	v_add_f32_e32 v2, v5, v2
	v_add_f32_e32 v2, v12, v2
	v_add_f32_e32 v15, v13, v2
	v_fma_f32 v2, v16, s70, -v149
	v_exp_f32_e32 v2, v2
	v_fma_f32 v3, v17, s70, -v149
	v_exp_f32_e32 v3, v3
	v_fma_f32 v10, v10, s70, -v149
	v_exp_f32_e32 v10, v10
	v_fma_f32 v11, v11, s70, -v149
	v_exp_f32_e32 v11, v11
	v_add_f32_e32 v15, v2, v15
	v_fma_f32 v8, v8, s70, -v149
	v_add_f32_e32 v15, v3, v15
	v_exp_f32_e32 v8, v8
	v_fma_f32 v9, v9, s70, -v149
	v_add_f32_e32 v15, v10, v15
	v_exp_f32_e32 v9, v9
	v_fma_f32 v14, v14, s70, -v149
	v_add_f32_e32 v16, v11, v15
	v_exp_f32_e32 v14, v14
	v_sub_f32_e32 v15, v148, v149
	v_exp_f32_e32 v15, v15
	v_add_f32_e32 v16, v8, v16
	v_add_f32_e32 v16, v9, v16
	v_add_f32_e32 v16, v14, v16
	v_add_f32_e32 v16, v15, v16
	v_mov_b32_e32 v17, v16
	s_nop 1
	v_permlane16_swap_b32_e32 v16, v17
	v_add_f32_e32 v16, v16, v17
	v_mov_b32_e32 v17, v16
	s_nop 1
	v_permlane32_swap_b32_e32 v16, v17
	s_and_saveexec_b64 s[22:23], s[4:5]
	v_add_f32_e32 v16, v16, v17
	ds_write_b32 v211, v16 offset:2816
	s_or_b64 exec, exec, s[22:23]
	s_waitcnt lgkmcnt(0)
	s_barrier
	ds_read_b128 v[222:225], v220
	ds_read_b128 v[226:229], v220 offset:256
	ds_read_b128 v[230:233], v220 offset:512
	v_lshl_add_u32 v114, s20, 8, v198
	v_lshl_or_b32 v16, s21, 8, v200
	v_ashrrev_i32_e32 v17, 31, v16
	s_cmp_eq_u32 s44, 3
	s_waitcnt lgkmcnt(2)
	s_nop 1
	v_mov_b32_e32 v146, v222
	v_mov_b32_e32 v147, v223
	v_mov_b32_e32 v148, v224
	v_mov_b32_e32 v149, v225
	ds_read_b128 v[222:225], v220 offset:768
	v_mov_b32_e32 v116, v147
	v_mov_b32_e32 v117, v148
	v_mov_b32_e32 v147, v149
	v_pk_add_f32 v[116:117], v[116:117], v[146:147]
	s_nop 0
	v_add_f32_e32 v115, v116, v117
	v_div_scale_f32 v116, s[20:21], v115, v115, 1.0
	v_rcp_f32_e32 v117, v116
	s_nop 0
	v_fma_f32 v146, -v116, v117, 1.0
	v_fmac_f32_e32 v117, v146, v117
	v_div_scale_f32 v146, vcc, 1.0, v115, 1.0
	v_mul_f32_e32 v147, v146, v117
	v_fma_f32 v148, -v116, v147, v146
	v_fmac_f32_e32 v147, v148, v117
	v_fma_f32 v116, -v116, v147, v146
	v_div_fmas_f32 v116, v116, v117, v147
	v_div_fixup_f32 v146, v116, v115, 1.0
	v_ashrrev_i32_e32 v115, 31, v114
	v_lshlrev_b64 v[116:117], 11, v[114:115]
	v_lshl_add_u64 v[148:149], s[30:31], 0, v[116:117]
	v_lshlrev_b64 v[116:117], 1, v[16:17]
	v_pk_mul_f32 v[120:121], v[120:121], v[146:147] op_sel_hi:[1,0]
	v_pk_mul_f32 v[118:119], v[118:119], v[146:147] op_sel_hi:[1,0]
	v_pk_mul_f32 v[124:125], v[124:125], v[146:147] op_sel_hi:[1,0]
	v_pk_mul_f32 v[122:123], v[122:123], v[146:147] op_sel_hi:[1,0]
	v_lshl_add_u64 v[16:17], v[148:149], 0, v[116:117]
	v_cvt_pk_bf16_f32 v118, v118, v119
	v_cvt_pk_bf16_f32 v119, v120, v121
	v_cvt_pk_bf16_f32 v120, v122, v123
	v_cvt_pk_bf16_f32 v121, v124, v125
	global_store_dwordx4 v[16:17], v[118:121], off
	v_pk_mul_f32 v[122:123], v[144:145], v[146:147] op_sel_hi:[1,0]
	v_pk_mul_f32 v[124:125], v[142:143], v[146:147] op_sel_hi:[1,0]
	v_pk_mul_f32 v[120:121], v[140:141], v[146:147] op_sel_hi:[1,0]
	v_pk_mul_f32 v[118:119], v[126:127], v[146:147] op_sel_hi:[1,0]
	s_nop 0
	v_cvt_pk_bf16_f32 v118, v118, v119
	v_cvt_pk_bf16_f32 v119, v120, v121
	v_cvt_pk_bf16_f32 v120, v124, v125
	v_cvt_pk_bf16_f32 v121, v122, v123
	global_store_dwordx4 v[16:17], v[118:121], off offset:256
	s_waitcnt lgkmcnt(2)
	s_nop 1
	v_mov_b32_e32 v118, v226
	v_mov_b32_e32 v119, v227
	v_mov_b32_e32 v120, v228
	v_mov_b32_e32 v121, v229
	ds_read_b128 v[226:229], v220 offset:2048
	v_mov_b32_e32 v122, v119
	v_mov_b32_e32 v123, v120
	v_mov_b32_e32 v119, v121
	v_pk_add_f32 v[118:119], v[122:123], v[118:119]
	s_nop 0
	v_add_f32_e32 v115, v118, v119
	v_div_scale_f32 v118, s[20:21], v115, v115, 1.0
	v_rcp_f32_e32 v119, v118
	s_nop 0
	v_fma_f32 v120, -v118, v119, 1.0
	v_fmac_f32_e32 v119, v120, v119
	v_div_scale_f32 v120, vcc, 1.0, v115, 1.0
	v_mul_f32_e32 v121, v120, v119
	v_fma_f32 v122, -v118, v121, v120
	v_fmac_f32_e32 v121, v122, v119
	v_fma_f32 v118, -v118, v121, v120
	v_or_b32_e32 v120, 16, v114
	v_div_fmas_f32 v118, v118, v119, v121
	v_ashrrev_i32_e32 v121, 31, v120
	v_div_fixup_f32 v118, v118, v115, 1.0
	v_lshlrev_b64 v[120:121], 11, v[120:121]
	v_lshl_add_u64 v[120:121], s[30:31], 0, v[120:121]
	v_pk_mul_f32 v[90:91], v[90:91], v[118:119] op_sel_hi:[1,0]
	v_pk_mul_f32 v[82:83], v[82:83], v[118:119] op_sel_hi:[1,0]
	v_pk_mul_f32 v[98:99], v[98:99], v[118:119] op_sel_hi:[1,0]
	v_pk_mul_f32 v[122:123], v[88:89], v[118:119] op_sel_hi:[1,0]
	v_lshl_add_u64 v[120:121], v[120:121], 0, v[116:117]
	v_cvt_pk_bf16_f32 v88, v82, v83
	v_cvt_pk_bf16_f32 v89, v90, v91
	v_cvt_pk_bf16_f32 v90, v122, v123
	v_cvt_pk_bf16_f32 v91, v98, v99
	global_store_dwordx4 v[120:121], v[88:91], off
	v_pk_mul_f32 v[82:83], v[96:97], v[118:119] op_sel_hi:[1,0]
	v_pk_mul_f32 v[86:87], v[86:87], v[118:119] op_sel_hi:[1,0]
	v_pk_mul_f32 v[90:91], v[106:107], v[118:119] op_sel_hi:[1,0]
	v_pk_mul_f32 v[88:89], v[100:101], v[118:119] op_sel_hi:[1,0]
	v_cvt_pk_bf16_f32 v86, v86, v87
	v_cvt_pk_bf16_f32 v87, v82, v83
	v_cvt_pk_bf16_f32 v88, v88, v89
	v_cvt_pk_bf16_f32 v89, v90, v91
	global_store_dwordx4 v[120:121], v[86:89], off offset:256
	s_waitcnt lgkmcnt(2)
; #define PG8_LAS __attribute__((address_space(3)))
; __device__ __forceinline__ unsigned cvt_pk_bf16(float lo, float hi) { const f32x2c v = {lo, hi}; const bf16x2c b = __builtin_convertvector(v, bf16x2c); return __builtin_bit_cast(unsigned, b); }
;     __device__ __forceinline__ void operator()(f32x4 (&acc)[2][2][4][2], const Unit& u, int wr, int wc, int fr, int fq) const {
;     ...
;         const int row0 = u.pm * BM + wr * 64 + fr, col0 = u.pn * 256 + wc * 32 + 8 * fq;
; #pragma unroll
;         for (int ai = 0; ai < 2; ++ai)
; #pragma unroll
;             for (int m = 0; m < 4; ++m) { const f32x4 q = *(const PG8_LAS f32x4*)(ssum + (ai * HALF + wr * 64 + m * 16 + fr) * 4);
;                 const float iv = 1.f / ((q[0] + q[1]) + (q[2] + q[3]));
;                 bf16* rowp = P + (size_t)(row0 + ai * HALF + m * 16) * D + col0;
; #pragma unroll
;                 for (int bj = 0; bj < 2; ++bj) { const f32x4 v0 = acc[ai][bj][m][0] * iv, v1 = acc[ai][bj][m][1] * iv; u32x4 w;
;                     w.x = cvt_pk_bf16(v0[0], v0[1]); w.y = cvt_pk_bf16(v0[2], v0[3]); w.z = cvt_pk_bf16(v1[0], v1[1]); w.w = cvt_pk_bf16(v1[2], v1[3]);
;                     *(u32x4*)(rowp + bj * HALF) = w; } }
	s_nop 1
	v_mov_b32_e32 v86, v230
	v_mov_b32_e32 v87, v231
	v_mov_b32_e32 v88, v232
	v_mov_b32_e32 v89, v233
	ds_read_b128 v[230:233], v220 offset:2304
	v_mov_b32_e32 v82, v87
	v_mov_b32_e32 v83, v88
	v_mov_b32_e32 v87, v89
	v_pk_add_f32 v[82:83], v[82:83], v[86:87]
	s_nop 0
	v_add_f32_e32 v82, v82, v83
	v_div_scale_f32 v83, s[20:21], v82, v82, 1.0
	v_rcp_f32_e32 v86, v83
	s_nop 0
	v_fma_f32 v87, -v83, v86, 1.0
	v_fmac_f32_e32 v86, v87, v86
	v_div_scale_f32 v87, vcc, 1.0, v82, 1.0
	v_mul_f32_e32 v88, v87, v86
	v_fma_f32 v89, -v83, v88, v87
	v_fmac_f32_e32 v88, v89, v86
	v_fma_f32 v83, -v83, v88, v87
	v_div_fmas_f32 v83, v83, v86, v88
	v_div_fixup_f32 v86, v83, v82, 1.0
	v_or_b32_e32 v82, 32, v114
	v_ashrrev_i32_e32 v83, 31, v82
	v_lshlrev_b64 v[82:83], 11, v[82:83]
	v_lshl_add_u64 v[82:83], s[30:31], 0, v[82:83]
	v_lshl_add_u64 v[88:89], v[82:83], 0, v[116:117]
	v_pk_mul_f32 v[90:91], v[92:93], v[86:87] op_sel_hi:[1,0]
	v_pk_mul_f32 v[82:83], v[84:85], v[86:87] op_sel_hi:[1,0]
	v_pk_mul_f32 v[92:93], v[102:103], v[86:87] op_sel_hi:[1,0]
	v_pk_mul_f32 v[84:85], v[94:95], v[86:87] op_sel_hi:[1,0]
	v_cvt_pk_bf16_f32 v82, v82, v83
	v_cvt_pk_bf16_f32 v83, v90, v91
	v_cvt_pk_bf16_f32 v84, v84, v85
	v_cvt_pk_bf16_f32 v85, v92, v93
	global_store_dwordx4 v[88:89], v[82:85], off
	v_pk_mul_f32 v[90:91], v[112:113], v[86:87] op_sel_hi:[1,0]
	s_nop 0
	v_pk_mul_f32 v[84:85], v[108:109], v[86:87] op_sel_hi:[1,0]
	v_pk_mul_f32 v[82:83], v[104:105], v[86:87] op_sel_hi:[1,0]
	v_pk_mul_f32 v[86:87], v[110:111], v[86:87] op_sel_hi:[1,0]
	v_cvt_pk_bf16_f32 v82, v82, v83
	v_cvt_pk_bf16_f32 v83, v84, v85
	v_cvt_pk_bf16_f32 v84, v86, v87
	v_cvt_pk_bf16_f32 v85, v90, v91
	global_store_dwordx4 v[88:89], v[82:85], off offset:256
	s_waitcnt lgkmcnt(2)
	s_nop 1
	v_mov_b32_e32 v82, v222
	v_mov_b32_e32 v83, v223
	v_mov_b32_e32 v84, v224
	v_mov_b32_e32 v85, v225
	ds_read_b128 v[222:225], v220 offset:2560
	v_mov_b32_e32 v86, v83
	v_mov_b32_e32 v87, v84
	v_mov_b32_e32 v83, v85
	v_pk_add_f32 v[82:83], v[86:87], v[82:83]
	s_nop 0
	v_add_f32_e32 v82, v82, v83
	v_div_scale_f32 v83, s[20:21], v82, v82, 1.0
	v_rcp_f32_e32 v84, v83
	s_nop 0
	v_fma_f32 v85, -v83, v84, 1.0
	v_fmac_f32_e32 v84, v85, v84
	v_div_scale_f32 v85, vcc, 1.0, v82, 1.0
	v_mul_f32_e32 v86, v85, v84
	v_fma_f32 v87, -v83, v86, v85
	v_fmac_f32_e32 v86, v87, v84
	v_fma_f32 v83, -v83, v86, v85
	v_div_fmas_f32 v83, v83, v84, v86
	v_or_b32_e32 v84, 48, v114
	v_ashrrev_i32_e32 v85, 31, v84
	v_div_fixup_f32 v82, v83, v82, 1.0
	v_lshlrev_b64 v[84:85], 11, v[84:85]
	v_lshl_add_u64 v[84:85], s[30:31], 0, v[84:85]
	v_pk_mul_f32 v[56:57], v[56:57], v[82:83] op_sel_hi:[1,0]
	v_pk_mul_f32 v[50:51], v[50:51], v[82:83] op_sel_hi:[1,0]
	v_pk_mul_f32 v[64:65], v[64:65], v[82:83] op_sel_hi:[1,0]
	v_pk_mul_f32 v[86:87], v[54:55], v[82:83] op_sel_hi:[1,0]
	v_lshl_add_u64 v[84:85], v[84:85], 0, v[116:117]
	v_cvt_pk_bf16_f32 v54, v50, v51
	v_cvt_pk_bf16_f32 v55, v56, v57
	v_cvt_pk_bf16_f32 v56, v86, v87
	v_cvt_pk_bf16_f32 v57, v64, v65
	global_store_dwordx4 v[84:85], v[54:57], off
	v_pk_mul_f32 v[50:51], v[52:53], v[82:83] op_sel_hi:[1,0]
	v_pk_mul_f32 v[52:53], v[68:69], v[82:83] op_sel_hi:[1,0]
	v_pk_mul_f32 v[54:55], v[62:63], v[82:83] op_sel_hi:[1,0]
	v_pk_mul_f32 v[56:57], v[74:75], v[82:83] op_sel_hi:[1,0]
	v_cvt_pk_bf16_f32 v50, v50, v51
	v_cvt_pk_bf16_f32 v51, v54, v55
	v_cvt_pk_bf16_f32 v52, v52, v53
	v_cvt_pk_bf16_f32 v53, v56, v57
	global_store_dwordx4 v[84:85], v[50:53], off offset:256
	v_lshl_add_u64 v[56:57], v[16:17], 0, s[58:59]
	s_waitcnt lgkmcnt(2)
	s_nop 1
	v_mov_b32_e32 v50, v226
	v_mov_b32_e32 v51, v227
	v_mov_b32_e32 v52, v228
	v_mov_b32_e32 v53, v229
	ds_read_b128 v[226:229], v220 offset:2816
	v_mov_b32_e32 v54, v51
	v_mov_b32_e32 v55, v52
	v_mov_b32_e32 v51, v53
	v_pk_add_f32 v[50:51], v[54:55], v[50:51]
	s_nop 0
	v_add_f32_e32 v50, v50, v51
	v_div_scale_f32 v51, s[20:21], v50, v50, 1.0
	v_rcp_f32_e32 v52, v51
	s_nop 0
	v_fma_f32 v53, -v51, v52, 1.0
	v_fmac_f32_e32 v52, v53, v52
	v_div_scale_f32 v53, vcc, 1.0, v50, 1.0
	v_mul_f32_e32 v54, v53, v52
	v_fma_f32 v55, -v51, v54, v53
	v_fmac_f32_e32 v54, v55, v52
	v_fma_f32 v51, -v51, v54, v53
	v_div_fmas_f32 v51, v51, v52, v54
	v_div_fixup_f32 v54, v51, v50, 1.0
	v_pk_mul_f32 v[52:53], v[60:61], v[54:55] op_sel_hi:[1,0]
	v_pk_mul_f32 v[50:51], v[58:59], v[54:55] op_sel_hi:[1,0]
	v_pk_mul_f32 v[58:59], v[72:73], v[54:55] op_sel_hi:[1,0]
	v_pk_mul_f32 v[60:61], v[66:67], v[54:55] op_sel_hi:[1,0]
	v_cvt_pk_bf16_f32 v50, v50, v51
	v_cvt_pk_bf16_f32 v51, v52, v53
	v_cvt_pk_bf16_f32 v53, v58, v59
	v_add_co_u32_e32 v58, vcc, s35, v16
	v_cvt_pk_bf16_f32 v52, v60, v61
	s_nop 0
	v_addc_co_u32_e32 v59, vcc, 0, v17, vcc
	global_store_dwordx4 v[58:59], v[50:53], off
	v_pk_mul_f32 v[58:59], v[80:81], v[54:55] op_sel_hi:[1,0]
	s_nop 0
	v_pk_mul_f32 v[52:53], v[76:77], v[54:55] op_sel_hi:[1,0]
	v_pk_mul_f32 v[50:51], v[70:71], v[54:55] op_sel_hi:[1,0]
	v_pk_mul_f32 v[54:55], v[78:79], v[54:55] op_sel_hi:[1,0]
	v_cvt_pk_bf16_f32 v50, v50, v51
	v_cvt_pk_bf16_f32 v51, v52, v53
	v_cvt_pk_bf16_f32 v52, v54, v55
	v_cvt_pk_bf16_f32 v53, v58, v59
	global_store_dwordx4 v[56:57], v[50:53], off offset:256
	s_waitcnt lgkmcnt(2)
; #define PG8_LAS __attribute__((address_space(3)))
; __device__ __forceinline__ unsigned cvt_pk_bf16(float lo, float hi) { const f32x2c v = {lo, hi}; const bf16x2c b = __builtin_convertvector(v, bf16x2c); return __builtin_bit_cast(unsigned, b); }
;     __device__ __forceinline__ void operator()(f32x4 (&acc)[2][2][4][2], const Unit& u, int wr, int wc, int fr, int fq) const {
;     ...
;         const int row0 = u.pm * BM + wr * 64 + fr, col0 = u.pn * 256 + wc * 32 + 8 * fq;
; #pragma unroll
;         for (int ai = 0; ai < 2; ++ai)
; #pragma unroll
;             for (int m = 0; m < 4; ++m) { const f32x4 q = *(const PG8_LAS f32x4*)(ssum + (ai * HALF + wr * 64 + m * 16 + fr) * 4);
;                 const float iv = 1.f / ((q[0] + q[1]) + (q[2] + q[3]));
;                 bf16* rowp = P + (size_t)(row0 + ai * HALF + m * 16) * D + col0;
; #pragma unroll
;                 for (int bj = 0; bj < 2; ++bj) { const f32x4 v0 = acc[ai][bj][m][0] * iv, v1 = acc[ai][bj][m][1] * iv; u32x4 w;
;                     w.x = cvt_pk_bf16(v0[0], v0[1]); w.y = cvt_pk_bf16(v0[2], v0[3]); w.z = cvt_pk_bf16(v1[0], v1[1]); w.w = cvt_pk_bf16(v1[2], v1[3]);
;                     *(u32x4*)(rowp + bj * HALF) = w; } }
	s_nop 1
	v_mov_b32_e32 v50, v230
	v_mov_b32_e32 v51, v231
	v_mov_b32_e32 v52, v232
	v_mov_b32_e32 v53, v233
	v_mov_b32_e32 v54, v51
	v_mov_b32_e32 v55, v52
	v_mov_b32_e32 v51, v53
	v_pk_add_f32 v[50:51], v[54:55], v[50:51]
	s_nop 0
	v_add_f32_e32 v50, v50, v51
	v_div_scale_f32 v51, s[20:21], v50, v50, 1.0
	v_rcp_f32_e32 v52, v51
	s_nop 0
	v_fma_f32 v53, -v51, v52, 1.0
	v_fmac_f32_e32 v52, v53, v52
	v_div_scale_f32 v53, vcc, 1.0, v50, 1.0
	v_mul_f32_e32 v54, v53, v52
	v_fma_f32 v55, -v51, v54, v53
	v_fmac_f32_e32 v54, v55, v52
	v_fma_f32 v51, -v51, v54, v53
	v_div_fmas_f32 v51, v51, v52, v54
	v_div_fixup_f32 v50, v51, v50, 1.0
	v_pk_mul_f32 v[18:19], v[18:19], v[50:51] op_sel_hi:[1,0]
	v_pk_mul_f32 v[26:27], v[26:27], v[50:51] op_sel_hi:[1,0]
	v_pk_mul_f32 v[36:37], v[36:37], v[50:51] op_sel_hi:[1,0]
	v_pk_mul_f32 v[54:55], v[24:25], v[50:51] op_sel_hi:[1,0]
	v_cvt_pk_bf16_f32 v24, v18, v19
	v_add_co_u32_e32 v18, vcc, s87, v16
	v_cvt_pk_bf16_f32 v25, v26, v27
	v_cvt_pk_bf16_f32 v26, v54, v55
	v_cvt_pk_bf16_f32 v27, v36, v37
	v_addc_co_u32_e32 v19, vcc, 0, v17, vcc
	global_store_dwordx4 v[18:19], v[24:27], off
	v_pk_mul_f32 v[18:19], v[20:21], v[50:51] op_sel_hi:[1,0]
	v_pk_mul_f32 v[20:21], v[34:35], v[50:51] op_sel_hi:[1,0]
	v_pk_mul_f32 v[24:25], v[30:31], v[50:51] op_sel_hi:[1,0]
	v_pk_mul_f32 v[26:27], v[42:43], v[50:51] op_sel_hi:[1,0]
	v_lshl_add_u64 v[52:53], v[16:17], 0, s[72:73]
	v_cvt_pk_bf16_f32 v18, v18, v19
	v_cvt_pk_bf16_f32 v19, v24, v25
	v_cvt_pk_bf16_f32 v20, v20, v21
	v_cvt_pk_bf16_f32 v21, v26, v27
	global_store_dwordx4 v[52:53], v[18:21], off offset:256
	v_lshl_add_u64 v[26:27], v[16:17], 0, s[74:75]
	s_waitcnt lgkmcnt(1)
	s_nop 1
	v_mov_b32_e32 v18, v222
	v_mov_b32_e32 v19, v223
	v_mov_b32_e32 v20, v224
	v_mov_b32_e32 v21, v225
	v_mov_b32_e32 v24, v19
	v_mov_b32_e32 v25, v20
	v_mov_b32_e32 v19, v21
	v_pk_add_f32 v[18:19], v[24:25], v[18:19]
	s_nop 0
	v_add_f32_e32 v18, v18, v19
	v_div_scale_f32 v19, s[20:21], v18, v18, 1.0
	v_rcp_f32_e32 v20, v19
	s_nop 0
	v_fma_f32 v21, -v19, v20, 1.0
	v_fmac_f32_e32 v20, v21, v20
	v_div_scale_f32 v21, vcc, 1.0, v18, 1.0
	v_mul_f32_e32 v24, v21, v20
	v_fma_f32 v25, -v19, v24, v21
	v_fmac_f32_e32 v24, v25, v20
	v_fma_f32 v19, -v19, v24, v21
	v_div_fmas_f32 v19, v19, v20, v24
	v_div_fixup_f32 v24, v19, v18, 1.0
	v_pk_mul_f32 v[20:21], v[28:29], v[24:25] op_sel_hi:[1,0]
	v_pk_mul_f32 v[18:19], v[22:23], v[24:25] op_sel_hi:[1,0]
	v_pk_mul_f32 v[22:23], v[40:41], v[24:25] op_sel_hi:[1,0]
	v_pk_mul_f32 v[28:29], v[32:33], v[24:25] op_sel_hi:[1,0]
	v_cvt_pk_bf16_f32 v18, v18, v19
	v_cvt_pk_bf16_f32 v19, v20, v21
	v_cvt_pk_bf16_f32 v21, v22, v23
	v_add_co_u32_e32 v22, vcc, s85, v16
	v_cvt_pk_bf16_f32 v20, v28, v29
	s_nop 0
	v_addc_co_u32_e32 v23, vcc, 0, v17, vcc
	global_store_dwordx4 v[22:23], v[18:21], off
	v_pk_mul_f32 v[22:23], v[48:49], v[24:25] op_sel_hi:[1,0]
	s_nop 0
	v_pk_mul_f32 v[20:21], v[44:45], v[24:25] op_sel_hi:[1,0]
	v_pk_mul_f32 v[18:19], v[38:39], v[24:25] op_sel_hi:[1,0]
	v_pk_mul_f32 v[24:25], v[46:47], v[24:25] op_sel_hi:[1,0]
	v_cvt_pk_bf16_f32 v18, v18, v19
	v_cvt_pk_bf16_f32 v19, v20, v21
	v_cvt_pk_bf16_f32 v20, v24, v25
	v_cvt_pk_bf16_f32 v21, v22, v23
	global_store_dwordx4 v[26:27], v[18:21], off offset:256
	s_waitcnt lgkmcnt(0)
	s_nop 1
	v_mov_b32_e32 v18, v226
	v_mov_b32_e32 v19, v227
	v_mov_b32_e32 v20, v228
	v_mov_b32_e32 v21, v229
	v_mov_b32_e32 v22, v19
	v_mov_b32_e32 v23, v20
	v_mov_b32_e32 v19, v21
	v_pk_add_f32 v[18:19], v[22:23], v[18:19]
	s_nop 0
	v_add_f32_e32 v18, v18, v19
	v_div_scale_f32 v19, s[20:21], v18, v18, 1.0
	v_rcp_f32_e32 v20, v19
	s_mov_b64 s[20:21], -1
	v_fma_f32 v21, -v19, v20, 1.0
	v_fmac_f32_e32 v20, v21, v20
	v_div_scale_f32 v21, vcc, 1.0, v18, 1.0
	v_mul_f32_e32 v22, v21, v20
	v_fma_f32 v23, -v19, v22, v21
	v_fmac_f32_e32 v22, v23, v20
	v_fma_f32 v19, -v19, v22, v21
	v_div_fmas_f32 v19, v19, v20, v22
	v_div_fixup_f32 v18, v19, v18, 1.0
	v_pk_mul_f32 v[0:1], v[0:1], v[18:19] op_sel_hi:[1,0]
	v_pk_mul_f32 v[6:7], v[6:7], v[18:19] op_sel_hi:[1,0]
	v_pk_mul_f32 v[12:13], v[12:13], v[18:19] op_sel_hi:[1,0]
	v_pk_mul_f32 v[22:23], v[4:5], v[18:19] op_sel_hi:[1,0]
	v_cvt_pk_bf16_f32 v4, v0, v1
	v_add_co_u32_e32 v0, vcc, s65, v16
	v_cvt_pk_bf16_f32 v5, v6, v7
	v_cvt_pk_bf16_f32 v6, v22, v23
	v_cvt_pk_bf16_f32 v7, v12, v13
	v_addc_co_u32_e32 v1, vcc, 0, v17, vcc
	global_store_dwordx4 v[0:1], v[4:7], off
	v_pk_mul_f32 v[0:1], v[2:3], v[18:19] op_sel_hi:[1,0]
	v_pk_mul_f32 v[2:3], v[8:9], v[18:19] op_sel_hi:[1,0]
	v_pk_mul_f32 v[4:5], v[10:11], v[18:19] op_sel_hi:[1,0]
	v_pk_mul_f32 v[6:7], v[14:15], v[18:19] op_sel_hi:[1,0]
	v_lshl_add_u64 v[20:21], v[16:17], 0, s[76:77]
	v_cvt_pk_bf16_f32 v0, v0, v1
	v_cvt_pk_bf16_f32 v1, v4, v5
	v_cvt_pk_bf16_f32 v2, v2, v3
	v_cvt_pk_bf16_f32 v3, v6, v7
	global_store_dwordx4 v[20:21], v[0:3], off offset:256
	s_cbranch_scc1 .LBB0_2066
	s_andn2_b64 vcc, exec, s[8:9]
	s_cbranch_vccnz .LBB0_2065
	s_barrier
	s_branch .LBB0_2065
